# speedup vs baseline: 1.0031x; 1.0031x over previous
_Z6k_partPKiPKfS2_S2_S2_S2_PiS3_PDF16_S4_S4_:
	s_cmpk_gt_i32 s2, 0x7a
	s_mov_b64 s[4:5], -1
	s_cbranch_scc0 .LBB0_60
	s_cmpk_gt_u32 s2, 0x1f4
	s_cbranch_scc0 .LBB0_53
	s_load_dwordx4 s[4:7], s[0:1], 0x10
	v_lshrrev_b32_e32 v1, 4, v0
	v_and_b32_e32 v3, 15, v0
	v_lshrrev_b32_e32 v2, 1, v0
	v_and_or_b32 v1, v1, 48, v3
	v_and_b32_e32 v4, 0x78, v2
	v_lshl_add_u32 v1, v1, 6, v4
	v_lshlrev_b32_e32 v4, 2, v1
	v_mov_b32_e32 v5, 0
	v_and_b32_e32 v8, 0x60, v2
	s_waitcnt lgkmcnt(0)
	v_lshl_add_u64 v[6:7], s[4:5], 0, v[4:5]
	v_subrev_u32_e32 v4, 64, v1
	v_lshl_add_u64 v[4:5], v[4:5], 2, s[6:7]
	v_cmp_gt_u32_e32 vcc, 64, v8
	s_load_dwordx2 s[4:5], s[0:1], 0x48
	s_movk_i32 s3, 0x80
	v_cndmask_b32_e32 v13, v5, v7, vcc
	v_cndmask_b32_e32 v12, v4, v6, vcc
	global_load_dwordx4 v[4:7], v[12:13], off offset:16
	global_load_dwordx4 v[8:11], v[12:13], off
	v_lshlrev_b32_e32 v1, 4, v0
	v_cmp_gt_u32_e32 vcc, s3, v0
	s_waitcnt vmcnt(1)
	v_cvt_pk_f16_f32 v7, v6, v7
	v_cvt_pk_f16_f32 v6, v4, v5
	s_waitcnt vmcnt(0)
	v_cvt_pk_f16_f32 v5, v10, v11
	v_cvt_pk_f16_f32 v4, v8, v9
	s_waitcnt lgkmcnt(0)
	global_store_dwordx4 v1, v[4:7], s[4:5]
	s_and_saveexec_b64 s[6:7], vcc
	s_cbranch_execz .LBB0_52
	s_load_dwordx4 s[8:11], s[0:1], 0x20
	v_lshrrev_b32_e32 v4, 2, v0
	v_and_b32_e32 v4, 12, v4
	v_and_or_b32 v2, v2, 32, v4
	v_cmp_lt_u32_e64 s[4:5], 1, v3
	v_cmp_gt_u32_e32 vcc, 4, v3
	v_lshlrev_b32_e32 v8, 6, v3
	s_and_saveexec_b64 s[12:13], s[4:5]
	s_xor_b64 s[12:13], exec, s[12:13]
	s_cbranch_execz .LBB0_7
	v_mov_b32_e32 v6, 0
	s_and_saveexec_b64 s[14:15], vcc
	s_cbranch_execz .LBB0_6
	v_add_lshl_u32 v3, v2, v8, 2
	s_waitcnt lgkmcnt(0)
	global_load_dword v6, v3, s[10:11] offset:-512

.Lk1c_a:
	s_mov_b64 exec, s[8:9]
	v_add_u32_e32 v33, 0x2f4000, v32
	v_add_u32_e32 v34, 0x5e8000, v32
	v_add_u32_e32 v35, 0x8dc000, v32
	v_add_u32_e32 v36, 0xbd0000, v32
	s_waitcnt vmcnt(0)
	v_cvt_pk_f16_f32 v2, v2, v3
	v_cvt_pk_f16_f32 v3, v4, v5
	global_store_dwordx2 v32, v[2:3], s[4:5]
	v_cvt_pk_f16_f32 v6, v6, v7
	v_cvt_pk_f16_f32 v7, v8, v9
	global_store_dwordx2 v33, v[6:7], s[4:5]
	v_cvt_pk_f16_f32 v10, v10, v11
	v_cvt_pk_f16_f32 v11, v12, v13
	global_store_dwordx2 v34, v[10:11], s[4:5]
	v_cvt_pk_f16_f32 v14, v14, v15
	v_cvt_pk_f16_f32 v15, v16, v17
	global_store_dwordx2 v35, v[14:15], s[4:5]
	s_and_saveexec_b64 s[8:9], vcc
	s_cbranch_execz .Lk1c_b
	v_cvt_pk_f16_f32 v18, v18, v19
	v_cvt_pk_f16_f32 v19, v20, v21
	global_store_dwordx2 v36, v[18:19], s[4:5]

amdhsa.kernels:
  - .agpr_count:     0
    .args:
      - .actual_access:  read_only
        .address_space:  global
        .offset:         0
        .size:           8
        .value_kind:     global_buffer
      - .actual_access:  read_only
        .address_space:  global
        .offset:         8
        .size:           8
        .value_kind:     global_buffer
      - .actual_access:  read_only
        .address_space:  global
        .offset:         16
        .size:           8
        .value_kind:     global_buffer
      - .actual_access:  read_only
        .address_space:  global
        .offset:         24
        .size:           8
        .value_kind:     global_buffer
      - .actual_access:  read_only
        .address_space:  global
        .offset:         32
        .size:           8
        .value_kind:     global_buffer
      - .actual_access:  read_only
        .address_space:  global
        .offset:         40
        .size:           8
        .value_kind:     global_buffer
      - .actual_access:  write_only
        .address_space:  global
        .offset:         48
        .size:           8
        .value_kind:     global_buffer
      - .actual_access:  write_only
        .address_space:  global
        .offset:         56
        .size:           8
        .value_kind:     global_buffer
      - .actual_access:  write_only
        .address_space:  global
        .offset:         64
        .size:           8
        .value_kind:     global_buffer
      - .actual_access:  write_only
        .address_space:  global
        .offset:         72
        .size:           8
        .value_kind:     global_buffer
      - .actual_access:  write_only
        .address_space:  global
        .offset:         80
        .size:           8
        .value_kind:     global_buffer
    .group_segment_fixed_size: 37120
    .kernarg_segment_align: 8
    .kernarg_segment_size: 88
    .language:       OpenCL C
    .language_version:
      - 2
      - 0
    .max_flat_workgroup_size: 1024
    .name:           _Z6k_partPKiPKfS2_S2_S2_S2_PiS3_PDF16_S4_S4_
    .private_segment_fixed_size: 0
    .sgpr_count:     28
    .sgpr_spill_count: 0
    .symbol:         _Z6k_partPKiPKfS2_S2_S2_S2_PiS3_PDF16_S4_S4_.kd
    .uniform_work_group_size: 1
    .uses_dynamic_stack: false
    .vgpr_count:     64
    .vgpr_spill_count: 0
    .wavefront_size: 64
  - .agpr_count:     0
    .args:
      - .actual_access:  read_only
        .address_space:  global
        .offset:         0
        .size:           8
        .value_kind:     global_buffer
      - .actual_access:  read_only
        .address_space:  global
        .offset:         8
        .size:           8
        .value_kind:     global_buffer
      - .actual_access:  read_only
        .address_space:  global
        .offset:         16
        .size:           8
        .value_kind:     global_buffer
      - .actual_access:  write_only
        .address_space:  global
        .offset:         24
        .size:           8
        .value_kind:     global_buffer
      - .address_space:  global
        .offset:         32
        .size:           8
        .value_kind:     global_buffer
      - .actual_access:  read_only
        .address_space:  global
        .offset:         40
        .size:           8
        .value_kind:     global_buffer
      - .actual_access:  read_only
        .address_space:  global
        .offset:         48
        .size:           8
        .value_kind:     global_buffer
      - .actual_access:  read_only
        .address_space:  global
        .offset:         56
        .size:           8
        .value_kind:     global_buffer
      - .actual_access:  read_only
        .address_space:  global
        .offset:         64
        .size:           8
        .value_kind:     global_buffer
      - .actual_access:  write_only
        .address_space:  global
        .offset:         72
        .size:           8
        .value_kind:     global_buffer
      - .actual_access:  write_only
        .address_space:  global
        .offset:         80
        .size:           8
        .value_kind:     global_buffer
    .group_segment_fixed_size: 38832
    .kernarg_segment_align: 8
    .kernarg_segment_size: 88
    .language:       OpenCL C
    .language_version:
      - 2
      - 0
    .max_flat_workgroup_size: 512
    .name:           _Z8k_layer1PKDF16_PKiS2_PiS3_PKDv4_jS6_PKfS8_P15HIP_vector_typeIfLj2EESB_
    .private_segment_fixed_size: 0
    .sgpr_count:     76
    .sgpr_spill_count: 0
    .symbol:         _Z8k_layer1PKDF16_PKiS2_PiS3_PKDv4_jS6_PKfS8_P15HIP_vector_typeIfLj2EESB_.kd
    .uniform_work_group_size: 1
    .uses_dynamic_stack: false
    .vgpr_count:     64
    .vgpr_spill_count: 0
    .wavefront_size: 64
  - .agpr_count:     0
    .args:
      - .actual_access:  read_only
        .address_space:  global
        .offset:         0
        .size:           8
        .value_kind:     global_buffer
      - .actual_access:  read_only
        .address_space:  global
        .offset:         8
        .size:           8
        .value_kind:     global_buffer
      - .actual_access:  read_only
        .address_space:  global
        .offset:         16
        .size:           8
        .value_kind:     global_buffer
      - .actual_access:  read_only
        .address_space:  global
        .offset:         24
        .size:           8
        .value_kind:     global_buffer
      - .actual_access:  write_only
        .address_space:  global
        .offset:         32
        .size:           8
        .value_kind:     global_buffer
    .group_segment_fixed_size: 0
    .kernarg_segment_align: 8
    .kernarg_segment_size: 40
    .language:       OpenCL C
    .language_version:
      - 2
      - 0
    .max_flat_workgroup_size: 448
    .name:           _Z8k_layer2PK15HIP_vector_typeIfLj2EES2_PKiS4_PS0_
    .private_segment_fixed_size: 0
    .sgpr_count:     21
    .sgpr_spill_count: 0
    .symbol:         _Z8k_layer2PK15HIP_vector_typeIfLj2EES2_PKiS4_PS0_.kd
    .uniform_work_group_size: 1
    .uses_dynamic_stack: false
    .vgpr_count:     25
    .vgpr_spill_count: 0
    .wavefront_size: 64
